# P3 loop3 software pipeline again, last-trip prefetch clamped instead of wrapped, on top of combo5
# baseline (speedup 1.0000x reference)
; #define GAS __attribute__((address_space(1)))
; __device__ __forceinline__ void unpack8(const u32x4 v, float (&f)[8]) { f[0] = bflo(v.x); f[1] = bfhi(v.x); f[2] = bflo(v.y); f[3] = bfhi(v.y); f[4] = bflo(v.z); f[5] = bfhi(v.z); f[6] = bflo(v.w); f[7] = bfhi(v.w); }
; __device__ __forceinline__ u32x4 pack8(const float (&f)[8]) { u32x4 o; o.x = cvtpk(f[0], f[1]); o.y = cvtpk(f[2], f[3]); o.z = cvtpk(f[4], f[5]); o.w = cvtpk(f[6], f[7]); return o; }
; __device__ __forceinline__ void p3_rows2(int row0, const bf16* PROJ, const float* sc_w, const float* sc_nw, const float* ssd_nw, const float* SSQ, bf16* Y, LAS unsigned char* scr, int lane) {
;     ...
;     for (int i = 0; i < 8; ++i) { const int c0 = (i * 64 + lane) * 8;
;         const float rg0 = 1.0f / sqrtf(__shfl(gs0, i * 8) * (1.f / 512.f) + EPS), rg1 = 1.0f / sqrtf(__shfl(gs1, i * 8) * (1.f / 512.f) + EPS);
;         float f0[8], f1[8]; unpack8(*(const GAS u32x4*)(yrow + i * 512), f0); unpack8(*(const GAS u32x4*)(yrow + D_MIX + i * 512), f1);
;         const f32x4 ga = *(const GAS f32x4*)(ssd_nw + c0), gb = *(const GAS f32x4*)(ssd_nw + c0 + 4); const float g[8] = {ga.x, ga.y, ga.z, ga.w, gb.x, gb.y, gb.z, gb.w};
; #pragma unroll
;         for (int j = 0; j < 8; ++j) { f0[j] *= rg0 * g[j]; f1[j] *= rg1 * g[j]; }
;         *(GAS u32x4*)(yrow + i * 512) = pack8(f0); *(GAS u32x4*)(yrow + D_MIX + i * 512) = pack8(f1); }
.LBB0_489:
	v_lshl_add_u64 v[34:35], v[24:25], 0, s[30:31]
	v_add_co_u32_e32 v42, vcc, s39, v34
	s_waitcnt vmcnt(8)
	v_mov_b32_e32 v6, v188
	v_mov_b32_e32 v7, v189
	v_mov_b32_e32 v8, v190
	v_mov_b32_e32 v9, v191
	v_addc_co_u32_e32 v43, vcc, 0, v35, vcc
	v_add_co_u32_e32 v44, vcc, s40, v34
	ds_bpermute_b32 v46, v31, v32
	s_nop 0
	v_addc_co_u32_e32 v45, vcc, 0, v35, vcc
	v_mov_b32_e32 v34, v192
	v_mov_b32_e32 v35, v193
	v_mov_b32_e32 v36, v194
	v_mov_b32_e32 v37, v195
	v_mov_b32_e32 v38, v196
	v_mov_b32_e32 v39, v197
	v_mov_b32_e32 v40, v198
	v_mov_b32_e32 v41, v199
	v_mov_b32_e32 v2, v184
	v_mov_b32_e32 v3, v185
	v_mov_b32_e32 v4, v186
	v_mov_b32_e32 v5, v187
	s_add_u32 s42, s30, 0x800
	s_min_u32 s42, s42, 0x1800
	s_add_u32 s44, s42, s39
	s_addc_u32 s45, 0, 0
	s_add_u32 s48, s42, s40
	s_addc_u32 s49, 0, 0
	s_lshl_b32 s42, s42, 1
	s_mov_b32 s43, 0
	v_lshl_add_u64 v[216:217], v[24:25], 0, s[44:45]
	v_lshl_add_u64 v[218:219], v[24:25], 0, s[48:49]
	v_lshl_add_u64 v[220:221], v[22:23], 0, s[42:43]
	global_load_dwordx4 v[184:187], v[220:221], off offset:-2048
	global_load_dwordx4 v[188:191], v[220:221], off offset:-2064
	global_load_dwordx4 v[192:195], v[216:217], off
	global_load_dwordx4 v[196:199], v[218:219], off
	ds_bpermute_b32 v47, v31, v33
	ds_bpermute_b32 v48, v31, v32 offset:32
	ds_bpermute_b32 v49, v31, v33 offset:32
	s_waitcnt lgkmcnt(3)
	v_fmamk_f32 v46, v46, 0x3b000000, v28
	v_mul_f32_e32 v50, 0x4f800000, v46
	s_waitcnt lgkmcnt(2)
	v_fmamk_f32 v47, v47, 0x3b000000, v28
	s_waitcnt lgkmcnt(1)
	v_fmamk_f32 v48, v48, 0x3b000000, v28
	v_cmp_gt_f32_e64 s[6:7], s36, v46
	v_mul_f32_e32 v51, 0x4f800000, v47
	v_cmp_gt_f32_e32 vcc, s36, v47
	v_mul_f32_e32 v52, 0x4f800000, v48
	v_cmp_gt_f32_e64 s[0:1], s36, v48
	v_cndmask_b32_e64 v46, v46, v50, s[6:7]
	s_waitcnt lgkmcnt(0)
	v_fmamk_f32 v49, v49, 0x3b000000, v28
	v_cndmask_b32_e32 v47, v47, v51, vcc
	v_cndmask_b32_e64 v48, v48, v52, s[0:1]
	v_sqrt_f32_e32 v50, v46
	v_mul_f32_e32 v53, 0x4f800000, v49
	v_cmp_gt_f32_e64 s[4:5], s36, v49
	v_sqrt_f32_e32 v51, v47
	v_sqrt_f32_e32 v52, v48
	v_cndmask_b32_e64 v49, v49, v53, s[4:5]
	v_sqrt_f32_e32 v53, v49
	v_add_u32_e32 v54, -1, v50
	v_add_u32_e32 v55, 1, v50
	v_add_u32_e32 v56, -1, v51
	v_add_u32_e32 v58, -1, v52
	v_fma_f32 v62, -v54, v50, v46
	v_add_u32_e32 v57, 1, v51
	v_add_u32_e32 v59, 1, v52
	v_fma_f32 v63, -v55, v50, v46
	v_fma_f32 v64, -v56, v51, v47
	v_fma_f32 v66, -v58, v52, v48
	v_cmp_ge_f32_e64 s[8:9], 0, v62
	v_add_u32_e32 v60, -1, v53
	v_fma_f32 v65, -v57, v51, v47
	v_fma_f32 v67, -v59, v52, v48
	v_cndmask_b32_e64 v50, v50, v54, s[8:9]
	v_cmp_ge_f32_e64 s[8:9], 0, v64
	v_cmp_ge_f32_e64 s[10:11], 0, v66
	v_cmp_lt_f32_e64 s[14:15], 0, v63
	v_add_u32_e32 v61, 1, v53
	v_fma_f32 v68, -v60, v53, v49
	v_cndmask_b32_e64 v51, v51, v56, s[8:9]
	v_cmp_lt_f32_e64 s[8:9], 0, v65
	v_cndmask_b32_e64 v52, v52, v58, s[10:11]
	v_cmp_lt_f32_e64 s[10:11], 0, v67
	v_cndmask_b32_e64 v50, v50, v55, s[14:15]
	v_fma_f32 v69, -v61, v53, v49
	v_cmp_ge_f32_e64 s[12:13], 0, v68
	v_cndmask_b32_e64 v51, v51, v57, s[8:9]
	v_cndmask_b32_e64 v52, v52, v59, s[10:11]
	v_mul_f32_e32 v54, 0x37800000, v50
	v_cndmask_b32_e64 v53, v53, v60, s[12:13]
	v_cmp_lt_f32_e64 s[12:13], 0, v69
	v_mul_f32_e32 v55, 0x37800000, v51
	v_mul_f32_e32 v56, 0x37800000, v52
	v_cndmask_b32_e64 v50, v50, v54, s[6:7]
	v_cmp_class_f32_e64 s[6:7], v46, v29
	v_cndmask_b32_e64 v53, v53, v61, s[12:13]
	v_cndmask_b32_e32 v51, v51, v55, vcc
	v_cmp_class_f32_e32 vcc, v47, v29
	v_cndmask_b32_e64 v52, v52, v56, s[0:1]
	v_cmp_class_f32_e64 s[0:1], v48, v29
	v_cndmask_b32_e64 v46, v50, v46, s[6:7]
	v_mul_f32_e32 v57, 0x37800000, v53
	v_cndmask_b32_e32 v47, v51, v47, vcc
	v_cndmask_b32_e64 v48, v52, v48, s[0:1]
	v_div_scale_f32 v50, s[0:1], v46, v46, 1.0
	v_cndmask_b32_e64 v53, v53, v57, s[4:5]
	v_div_scale_f32 v52, s[0:1], v47, v47, 1.0
	v_rcp_f32_e32 v57, v50
	v_rcp_f32_e32 v58, v52
	v_cmp_class_f32_e64 s[4:5], v49, v29
	v_div_scale_f32 v51, vcc, 1.0, v46, 1.0
	v_fma_f32 v59, -v50, v57, 1.0
	v_fma_f32 v60, -v52, v58, 1.0
	v_fmac_f32_e32 v57, v59, v57
	v_cndmask_b32_e64 v49, v53, v49, s[4:5]
	v_div_scale_f32 v53, s[4:5], 1.0, v47, 1.0
	v_fmac_f32_e32 v58, v60, v58
	v_mul_f32_e32 v59, v51, v57
	v_mul_f32_e32 v60, v53, v58
	v_fma_f32 v61, -v50, v59, v51
	v_fma_f32 v62, -v52, v60, v53
	v_fmac_f32_e32 v59, v61, v57
	v_fmac_f32_e32 v60, v62, v58
	v_fma_f32 v50, -v50, v59, v51
	v_fma_f32 v51, -v52, v60, v53
	v_div_fmas_f32 v50, v50, v57, v59
	s_mov_b64 vcc, s[4:5]
	v_div_fixup_f32 v46, v50, v46, 1.0
	v_div_fmas_f32 v50, v51, v58, v60
	v_div_fixup_f32 v47, v50, v47, 1.0
	s_nop 0
	v_mul_f32_e32 v50, v46, v6
	v_mul_f32_e32 v6, v6, v47
	v_mul_f32_e32 v51, v46, v7
	v_mul_f32_e32 v7, v7, v47
	v_mul_f32_e32 v52, v46, v8
	v_mul_f32_e32 v8, v8, v47
	v_mul_f32_e32 v53, v46, v9
	v_mul_f32_e32 v9, v9, v47
	v_mul_f32_e32 v57, v46, v2
	v_mul_f32_e32 v2, v47, v2
	v_mul_f32_e32 v58, v46, v3
	v_mul_f32_e32 v3, v47, v3
	v_mul_f32_e32 v59, v46, v4
	v_mul_f32_e32 v4, v47, v4
	v_mul_f32_e32 v46, v46, v5
	v_mul_f32_e32 v5, v47, v5
	s_nop 0
	v_lshlrev_b32_e32 v47, 16, v34
	v_and_b32_e32 v34, 0xffff0000, v34
	v_lshlrev_b32_e32 v60, 16, v35
	v_and_b32_e32 v35, 0xffff0000, v35
	v_lshlrev_b32_e32 v61, 16, v36
	v_and_b32_e32 v36, 0xffff0000, v36
	v_lshlrev_b32_e32 v62, 16, v37
	v_and_b32_e32 v37, 0xffff0000, v37
	s_nop 0
	v_lshlrev_b32_e32 v63, 16, v38
	v_and_b32_e32 v38, 0xffff0000, v38
	v_lshlrev_b32_e32 v64, 16, v39
	v_and_b32_e32 v39, 0xffff0000, v39
	v_lshlrev_b32_e32 v65, 16, v40
	v_and_b32_e32 v40, 0xffff0000, v40
	v_lshlrev_b32_e32 v66, 16, v41
	v_and_b32_e32 v41, 0xffff0000, v41
	v_mul_f32_e32 v47, v50, v47
	v_mul_f32_e32 v34, v51, v34
	v_mul_f32_e32 v7, v7, v38
	v_mul_f32_e32 v38, v52, v60
	v_mul_f32_e32 v35, v53, v35
	v_mul_f32_e32 v9, v9, v39
	v_mul_f32_e32 v39, v57, v61
	v_mul_f32_e32 v50, v2, v65
	v_mul_f32_e32 v36, v58, v36
	v_mul_f32_e32 v40, v3, v40
	v_mul_f32_e32 v51, v59, v62
	v_mul_f32_e32 v52, v4, v66
	v_mul_f32_e32 v37, v46, v37
	v_mul_f32_e32 v41, v5, v41
	v_cvt_pk_bf16_f32 v2, v47, v34
	v_cvt_pk_bf16_f32 v3, v38, v35
	v_cvt_pk_bf16_f32 v4, v39, v36
	v_cvt_pk_bf16_f32 v5, v51, v37
	v_mul_f32_e32 v6, v6, v63
	v_mul_f32_e32 v8, v8, v64
	global_store_dwordx4 v[42:43], v[2:5], off
	v_div_scale_f32 v54, s[0:1], v48, v48, 1.0
	s_nop 0
	v_cvt_pk_bf16_f32 v2, v6, v7
	v_cvt_pk_bf16_f32 v3, v8, v9
	v_cvt_pk_bf16_f32 v4, v50, v40
	v_cvt_pk_bf16_f32 v5, v52, v41
	global_store_dwordx4 v[44:45], v[2:5], off
	s_waitcnt vmcnt(8)
; #define GAS __attribute__((address_space(1)))
; __device__ __forceinline__ void unpack8(const u32x4 v, float (&f)[8]) { f[0] = bflo(v.x); f[1] = bfhi(v.x); f[2] = bflo(v.y); f[3] = bfhi(v.y); f[4] = bflo(v.z); f[5] = bfhi(v.z); f[6] = bflo(v.w); f[7] = bfhi(v.w); }
; __device__ __forceinline__ u32x4 pack8(const float (&f)[8]) { u32x4 o; o.x = cvtpk(f[0], f[1]); o.y = cvtpk(f[2], f[3]); o.z = cvtpk(f[4], f[5]); o.w = cvtpk(f[6], f[7]); return o; }
; __device__ __forceinline__ void p3_rows2(int row0, const bf16* PROJ, const float* sc_w, const float* sc_nw, const float* ssd_nw, const float* SSQ, bf16* Y, LAS unsigned char* scr, int lane) {
;     ...
;     for (int i = 0; i < 8; ++i) { const int c0 = (i * 64 + lane) * 8;
;         const float rg0 = 1.0f / sqrtf(__shfl(gs0, i * 8) * (1.f / 512.f) + EPS), rg1 = 1.0f / sqrtf(__shfl(gs1, i * 8) * (1.f / 512.f) + EPS);
;         float f0[8], f1[8]; unpack8(*(const GAS u32x4*)(yrow + i * 512), f0); unpack8(*(const GAS u32x4*)(yrow + D_MIX + i * 512), f1);
;         const f32x4 ga = *(const GAS f32x4*)(ssd_nw + c0), gb = *(const GAS f32x4*)(ssd_nw + c0 + 4); const float g[8] = {ga.x, ga.y, ga.z, ga.w, gb.x, gb.y, gb.z, gb.w};
; #pragma unroll
;         for (int j = 0; j < 8; ++j) { f0[j] *= rg0 * g[j]; f1[j] *= rg1 * g[j]; }
;         *(GAS u32x4*)(yrow + i * 512) = pack8(f0); *(GAS u32x4*)(yrow + D_MIX + i * 512) = pack8(f1); }
; __global__ void __launch_bounds__(NWAVES * 64, 2) mk_fwd(Args args) {
;     ...
;         for (int m2 = gw; m2 < M / 2; m2 += NGW) p3_rows2(2 * m2, PROJ, sc_conv_w, sc_norm_w, ssd_norm_w, SSQ, Y, lds + RING_OFF + wave * 16384, lane);
	v_mov_b32_e32 v6, v200
	v_mov_b32_e32 v7, v201
	v_mov_b32_e32 v8, v202
	v_mov_b32_e32 v9, v203
	s_nop 0
	v_mov_b32_e32 v2, v204
	v_mov_b32_e32 v3, v205
	v_mov_b32_e32 v4, v206
	v_mov_b32_e32 v5, v207
	v_mov_b32_e32 v34, v208
	v_mov_b32_e32 v35, v209
	v_mov_b32_e32 v36, v210
	v_mov_b32_e32 v37, v211
	v_mov_b32_e32 v38, v212
	v_mov_b32_e32 v39, v213
	v_mov_b32_e32 v40, v214
	v_mov_b32_e32 v41, v215
	global_load_dwordx4 v[200:203], v[216:217], off offset:1024
	global_load_dwordx4 v[204:207], v[220:221], off
	global_load_dwordx4 v[208:211], v[220:221], off offset:-16
	global_load_dwordx4 v[212:215], v[218:219], off offset:1024
	v_div_scale_f32 v56, s[6:7], v49, v49, 1.0
	v_rcp_f32_e32 v47, v54
	v_rcp_f32_e32 v50, v56
	v_div_scale_f32 v55, s[0:1], 1.0, v48, 1.0
	v_fma_f32 v51, -v54, v47, 1.0
	v_fma_f32 v52, -v56, v50, 1.0
	v_fmac_f32_e32 v47, v51, v47
	v_div_scale_f32 v46, s[4:5], 1.0, v49, 1.0
	v_fmac_f32_e32 v50, v52, v50
	v_mul_f32_e32 v51, v55, v47
	v_mul_f32_e32 v52, v46, v50
	v_fma_f32 v53, -v54, v51, v55
	v_fma_f32 v57, -v56, v52, v46
	v_fmac_f32_e32 v51, v53, v47
	v_fmac_f32_e32 v52, v57, v50
	v_fma_f32 v53, -v54, v51, v55
	s_mov_b64 vcc, s[0:1]
	v_fma_f32 v46, -v56, v52, v46
	v_div_fmas_f32 v47, v53, v47, v51
	s_mov_b64 vcc, s[4:5]
	v_div_fmas_f32 v46, v46, v50, v52
	s_add_u32 s30, s30, 0x800
	v_div_fixup_f32 v47, v47, v48, 1.0
	v_div_fixup_f32 v46, v46, v49, 1.0
	s_addc_u32 s31, s31, 0
	v_add_u32_e32 v31, 64, v31
	s_cmpk_lg_i32 s30, 0x2000
	v_lshl_add_u64 v[26:27], v[26:27], 0, s[26:27]
	s_nop 0
	v_mul_f32_e32 v60, v47, v2
	v_lshlrev_b32_e32 v48, 16, v6
	v_and_b32_e32 v6, 0xffff0000, v6
	v_lshlrev_b32_e32 v49, 16, v7
	v_and_b32_e32 v7, 0xffff0000, v7
	v_lshlrev_b32_e32 v50, 16, v8
	v_and_b32_e32 v8, 0xffff0000, v8
	v_lshlrev_b32_e32 v51, 16, v9
	v_and_b32_e32 v9, 0xffff0000, v9
	s_nop 0
	v_lshlrev_b32_e32 v52, 16, v38
	v_and_b32_e32 v38, 0xffff0000, v38
	v_lshlrev_b32_e32 v53, 16, v39
	v_and_b32_e32 v39, 0xffff0000, v39
	v_lshlrev_b32_e32 v54, 16, v40
	v_and_b32_e32 v40, 0xffff0000, v40
	v_lshlrev_b32_e32 v55, 16, v41
	v_and_b32_e32 v41, 0xffff0000, v41
	v_mul_f32_e32 v56, v47, v34
	v_mul_f32_e32 v57, v47, v35
	v_mul_f32_e32 v35, v35, v46
	v_mul_f32_e32 v58, v47, v36
	v_mul_f32_e32 v59, v47, v37
	v_mul_f32_e32 v37, v37, v46
	v_mul_f32_e32 v2, v46, v2
	v_mul_f32_e32 v61, v47, v3
	v_mul_f32_e32 v3, v46, v3
	v_mul_f32_e32 v62, v47, v4
	v_mul_f32_e32 v4, v46, v4
	v_mul_f32_e32 v47, v47, v5
	v_mul_f32_e32 v5, v46, v5
	v_mul_f32_e32 v34, v34, v46
	v_mul_f32_e32 v36, v36, v46
	v_mul_f32_e32 v46, v56, v48
	v_mul_f32_e32 v6, v57, v6
	v_mul_f32_e32 v35, v35, v38
	v_mul_f32_e32 v38, v58, v49
	v_mul_f32_e32 v7, v59, v7
	v_mul_f32_e32 v37, v37, v39
	v_mul_f32_e32 v39, v60, v50
	v_mul_f32_e32 v48, v2, v54
	v_mul_f32_e32 v8, v61, v8
	v_mul_f32_e32 v40, v3, v40
	v_mul_f32_e32 v49, v62, v51
	v_mul_f32_e32 v50, v4, v55
	v_mul_f32_e32 v9, v47, v9
	v_mul_f32_e32 v41, v5, v41
	v_cvt_pk_bf16_f32 v2, v46, v6
	v_cvt_pk_bf16_f32 v3, v38, v7
	v_cvt_pk_bf16_f32 v4, v39, v8
	v_cvt_pk_bf16_f32 v5, v49, v9
	v_mul_f32_e32 v34, v34, v52
	v_mul_f32_e32 v36, v36, v53
	global_store_dwordx4 v[42:43], v[2:5], off offset:1024
	s_nop 1
	v_cvt_pk_bf16_f32 v2, v34, v35
	v_cvt_pk_bf16_f32 v3, v36, v37
	v_cvt_pk_bf16_f32 v4, v48, v40
	v_cvt_pk_bf16_f32 v5, v50, v41
	global_store_dwordx4 v[44:45], v[2:5], off offset:1024
	s_cbranch_scc1 .LBB0_489
	s_add_i32 s41, s41, s46
	s_add_i32 s16, s16, s33
	s_cmpk_gt_i32 s41, 0x1fff
	s_cbranch_scc0 .LBB0_484
